# P1: xor-8/4/2/1 steps of the row sum-of-squares and abs-max butterflies as DPP moves (bit-identical)
# speedup vs baseline: 1.0014x; 1.0014x over previous
.LBB0_104:
	s_waitcnt lgkmcnt(5)
	global_load_dwordx4 v[6:9], v[42:43], off offset:-4096
	s_waitcnt lgkmcnt(3)
	global_load_dwordx4 v[10:13], v[42:43], off offset:-3072
	s_waitcnt lgkmcnt(0)
	global_load_dwordx4 v[18:21], v[42:43], off offset:-2048
	global_load_dwordx4 v[22:25], v[42:43], off offset:-1024
	global_load_dwordx4 v[30:33], v[42:43], off
	global_load_dwordx4 v[26:29], v[42:43], off offset:1024
	global_load_dwordx4 v[14:17], v[42:43], off offset:2048
	global_load_dwordx4 v[2:5], v[42:43], off offset:3072
	v_cmp_lt_i32_e32 vcc, v63, v62
	s_mov_b32 s82, 0x800000
	s_and_b32 s75, s0, 0xffffe000
	v_cndmask_b32_e32 v45, v34, v63, vcc
	v_lshlrev_b32_e32 v45, 2, v45
	v_cmp_lt_i32_e32 vcc, v64, v62
	v_add_u32_e32 v78, s75, v61
	s_waitcnt vmcnt(7)
	v_mul_f32_e32 v74, v7, v7
	s_waitcnt vmcnt(6)
	v_mul_f32_e32 v75, v11, v11
	s_waitcnt vmcnt(5)
	v_mul_f32_e32 v76, v19, v19
	v_fmac_f32_e32 v74, v6, v6
	s_waitcnt vmcnt(3)
	v_mov_b32_e32 v48, v31
	s_waitcnt vmcnt(2)
	v_mov_b32_e32 v49, v27
	v_fmac_f32_e32 v75, v10, v10
	v_mul_f32_e32 v77, v23, v23
	v_mov_b32_e32 v46, v30
	v_mov_b32_e32 v47, v26
	v_fmac_f32_e32 v76, v18, v18
	v_pk_mul_f32 v[48:49], v[48:49], v[48:49]
	v_fmac_f32_e32 v74, v8, v8
	v_fmac_f32_e32 v75, v12, v12
	v_mov_b32_e32 v50, v32
	v_mov_b32_e32 v51, v28
	v_fmac_f32_e32 v77, v22, v22
	v_fmac_f32_e32 v76, v20, v20
	v_pk_fma_f32 v[46:47], v[46:47], v[46:47], v[48:49]
	v_fmac_f32_e32 v74, v9, v9
	v_fmac_f32_e32 v75, v13, v13
	s_waitcnt vmcnt(1)
	v_mov_b32_e32 v56, v15
	s_waitcnt vmcnt(0)
	v_mov_b32_e32 v57, v3
	v_fmac_f32_e32 v77, v24, v24
	v_fmac_f32_e32 v76, v21, v21
	v_pk_fma_f32 v[46:47], v[50:51], v[50:51], v[46:47]
	v_add_f32_e32 v50, v74, v75
	v_mov_b32_e32 v52, v33
	v_mov_b32_e32 v53, v29
	v_mov_b32_e32 v54, v14
	v_mov_b32_e32 v55, v2
	v_pk_mul_f32 v[56:57], v[56:57], v[56:57]
	v_fmac_f32_e32 v77, v25, v25
	v_add_f32_e32 v50, v50, v76
	v_mov_b32_e32 v58, v16
	v_mov_b32_e32 v59, v4
	v_pk_fma_f32 v[48:49], v[54:55], v[54:55], v[56:57]
	v_pk_fma_f32 v[46:47], v[52:53], v[52:53], v[46:47]
	v_add_f32_e32 v50, v50, v77
	v_mov_b32_e32 v72, v17
	v_mov_b32_e32 v73, v5
	v_pk_fma_f32 v[48:49], v[58:59], v[58:59], v[48:49]
	v_add_f32_e32 v46, v50, v46
	v_pk_fma_f32 v[48:49], v[72:73], v[72:73], v[48:49]
	v_add_f32_e32 v46, v46, v47
	v_add_f32_e32 v46, v46, v48
	v_add_f32_e32 v46, v46, v49
	ds_bpermute_b32 v47, v45, v46
	v_cndmask_b32_e32 v48, v34, v64, vcc
	v_lshlrev_b32_e32 v72, 2, v48
	v_cmp_lt_i32_e32 vcc, v65, v62
	v_add_u32_e32 v77, s75, v60
	s_waitcnt lgkmcnt(0)
	v_add_f32_e32 v46, v46, v47
	ds_bpermute_b32 v47, v72, v46
	v_cndmask_b32_e32 v49, v34, v65, vcc
	v_lshlrev_b32_e32 v73, 2, v49
	v_cmp_lt_i32_e32 vcc, v66, v62
	ds_read_b128 v[80:83], v77
	ds_read_b128 v[84:87], v77 offset:1024
	ds_read_b128 v[88:91], v78
	ds_read_b128 v[92:95], v78 offset:1024
	s_waitcnt lgkmcnt(4)
	v_add_f32_e32 v46, v46, v47
	s_nop 1
	v_mov_b32_dpp v47, v46 row_ror:8 row_mask:0xf bank_mask:0xf
	v_cndmask_b32_e32 v48, v34, v66, vcc
	v_lshlrev_b32_e32 v76, 2, v48
	v_cmp_lt_i32_e32 vcc, v67, v62
	ds_read_b128 v[96:99], v77 offset:2048
	ds_read_b128 v[100:103], v77 offset:3072
	ds_read_b128 v[104:107], v78 offset:2048
	ds_read_b128 v[108:111], v78 offset:3072
	s_waitcnt lgkmcnt(4)
	v_add_f32_e32 v46, v46, v47
	s_nop 1
	v_mov_b32_dpp v47, v46 row_ror:4 row_mask:0xf bank_mask:0xf
	v_cndmask_b32_e32 v50, v34, v67, vcc
	v_lshlrev_b32_e32 v75, 2, v50
	v_cmp_lt_i32_e32 vcc, v68, v62
	ds_read_b128 v[112:115], v77 offset:4096
	ds_read_b128 v[116:119], v77 offset:5120
	ds_read_b128 v[120:123], v78 offset:4096
	ds_read_b128 v[124:127], v78 offset:5120
	s_waitcnt lgkmcnt(4)
	v_add_f32_e32 v46, v46, v47
	s_nop 1
	v_mov_b32_dpp v47, v46 quad_perm:[2,3,0,1] row_mask:0xf bank_mask:0xf
	v_cndmask_b32_e32 v49, v34, v68, vcc
	v_lshlrev_b32_e32 v74, 2, v49
	s_waitcnt lgkmcnt(0)
	v_add_f32_e32 v46, v46, v47
	s_nop 1
	v_mov_b32_dpp v47, v46 quad_perm:[1,0,3,2] row_mask:0xf bank_mask:0xf
	s_waitcnt lgkmcnt(0)
	v_add_f32_e32 v46, v46, v47
	v_fmamk_f32 v46, v46, 0x3a000000, v69
	v_mul_f32_e32 v47, 0x4b800000, v46
	v_cmp_gt_f32_e32 vcc, s82, v46
	s_nop 1
	v_cndmask_b32_e32 v46, v46, v47, vcc
	v_rsq_f32_e32 v46, v46
	s_nop 0
	v_mul_f32_e32 v47, 0x45800000, v46
	v_cndmask_b32_e32 v128, v46, v47, vcc
	v_pk_mul_f32 v[56:57], v[8:9], v[128:129] op_sel_hi:[1,0]
	v_pk_mul_f32 v[58:59], v[6:7], v[128:129] op_sel_hi:[1,0]
	v_pk_mul_f32 v[52:53], v[12:13], v[128:129] op_sel_hi:[1,0]
	v_pk_mul_f32 v[54:55], v[10:11], v[128:129] op_sel_hi:[1,0]
	v_pk_fma_f32 v[6:7], v[82:83], v[56:57], v[90:91]
	v_pk_fma_f32 v[8:9], v[80:81], v[58:59], v[88:89]
	v_pk_mul_f32 v[48:49], v[20:21], v[128:129] op_sel_hi:[1,0]
	v_pk_mul_f32 v[50:51], v[18:19], v[128:129] op_sel_hi:[1,0]
	v_pk_mul_f32 v[18:19], v[26:27], v[128:129] op_sel_hi:[1,0]
	v_pk_fma_f32 v[10:11], v[86:87], v[52:53], v[94:95]
	v_pk_fma_f32 v[26:27], v[84:85], v[54:55], v[92:93]
	v_max_f32_e64 v8, |v8|, |v9|
	v_max_f32_e64 v6, |v6|, |v7|
	v_pk_mul_f32 v[24:25], v[24:25], v[128:129] op_sel_hi:[1,0]
	v_pk_mul_f32 v[46:47], v[22:23], v[128:129] op_sel_hi:[1,0]
	v_pk_mul_f32 v[22:23], v[30:31], v[128:129] op_sel_hi:[1,0]
	v_pk_mul_f32 v[12:13], v[28:29], v[128:129] op_sel_hi:[1,0]
	v_pk_fma_f32 v[28:29], v[98:99], v[48:49], v[106:107]
	v_pk_fma_f32 v[30:31], v[96:97], v[50:51], v[104:105]
	v_max_f32_e64 v7, |v26|, |v27|
	v_max_f32_e64 v9, |v10|, |v11|
	v_max3_f32 v6, v8, 0, v6
	v_pk_mul_f32 v[20:21], v[32:33], v[128:129] op_sel_hi:[1,0]
	v_pk_fma_f32 v[32:33], v[102:103], v[24:25], v[110:111]
	v_pk_fma_f32 v[80:81], v[100:101], v[46:47], v[108:109]
	v_max_f32_e64 v10, |v30|, |v31|
	v_max_f32_e64 v11, |v28|, |v29|
	v_max3_f32 v6, v6, v7, v9
	v_pk_fma_f32 v[82:83], v[114:115], v[20:21], v[122:123]
	v_pk_fma_f32 v[84:85], v[112:113], v[22:23], v[120:121]
	v_max_f32_e64 v26, |v80|, |v81|
	v_max_f32_e64 v27, |v32|, |v33|
	v_max3_f32 v6, v6, v10, v11
	v_max_f32_e64 v28, |v84|, |v85|
	v_max_f32_e64 v29, |v82|, |v83|
	v_max3_f32 v6, v6, v26, v27
	v_max3_f32 v10, v6, v28, v29
	ds_read_b128 v[26:29], v77 offset:6144
	ds_read_b128 v[30:33], v78 offset:6144
	v_pk_fma_f32 v[6:7], v[118:119], v[12:13], v[126:127]
	v_pk_fma_f32 v[8:9], v[116:117], v[18:19], v[124:125]
	v_max_f32_e64 v6, |v6|, |v7|
	v_max_f32_e64 v8, |v8|, |v9|
	v_max3_f32 v79, v10, v8, v6
	v_pk_mul_f32 v[8:9], v[16:17], v[128:129] op_sel_hi:[1,0]
	v_pk_mul_f32 v[10:11], v[14:15], v[128:129] op_sel_hi:[1,0]
	ds_read_b128 v[14:17], v77 offset:7168
	ds_read_b128 v[80:83], v78 offset:7168
	s_waitcnt lgkmcnt(2)
	v_pk_fma_f32 v[6:7], v[28:29], v[8:9], v[32:33]
	v_pk_fma_f32 v[26:27], v[26:27], v[10:11], v[30:31]
	v_max_f32_e64 v6, |v6|, |v7|
	v_max_f32_e64 v26, |v26|, |v27|
	v_max3_f32 v26, v79, v26, v6
	v_pk_mul_f32 v[4:5], v[4:5], v[128:129] op_sel_hi:[1,0]
	v_pk_mul_f32 v[6:7], v[2:3], v[128:129] op_sel_hi:[1,0]
	s_waitcnt lgkmcnt(0)
	v_pk_fma_f32 v[2:3], v[4:5], v[16:17], v[82:83]
	v_pk_fma_f32 v[14:15], v[6:7], v[14:15], v[80:81]
	v_max_f32_e64 v2, |v2|, |v3|
	v_max_f32_e64 v14, |v14|, |v15|
	v_max3_f32 v2, v26, v14, v2
	ds_bpermute_b32 v3, v45, v2
	s_waitcnt lgkmcnt(0)
	v_max_f32_e32 v3, v3, v3
	v_max_f32_e32 v2, v2, v3
	ds_bpermute_b32 v3, v72, v2
	s_waitcnt lgkmcnt(0)
	v_max_f32_e32 v3, v3, v3
	v_max_f32_e32 v2, v2, v3
	s_nop 1
	v_mov_b32_dpp v3, v2 row_ror:8 row_mask:0xf bank_mask:0xf
	s_waitcnt lgkmcnt(0)
	v_max_f32_e32 v3, v3, v3
	v_max_f32_e32 v2, v2, v3
	s_nop 1
	v_mov_b32_dpp v3, v2 row_ror:4 row_mask:0xf bank_mask:0xf
	s_waitcnt lgkmcnt(0)
	v_max_f32_e32 v3, v3, v3
	v_max_f32_e32 v2, v2, v3
	s_nop 1
	v_mov_b32_dpp v3, v2 quad_perm:[2,3,0,1] row_mask:0xf bank_mask:0xf
	s_waitcnt lgkmcnt(0)
	v_max_f32_e32 v3, v3, v3
	v_max_f32_e32 v2, v2, v3
	s_nop 1
	v_mov_b32_dpp v3, v2 quad_perm:[1,0,3,2] row_mask:0xf bank_mask:0xf
	s_waitcnt lgkmcnt(0)
	v_max_f32_e32 v3, v3, v3
	v_max_f32_e32 v2, v2, v3
	s_and_saveexec_b64 s[82:83], s[6:7]
	s_cbranch_execz .LBB0_106
	s_add_u32 s86, s76, s25
	s_addc_u32 s87, s77, s34
	v_mul_f32_e32 v3, 0x3c010204, v2
	global_store_dword v35, v3, s[86:87]
